# attention QK stage re-emitted with 16 K-gather loads in flight (rolling refill) instead of hipcc's 2-deep serialized gathers; on top of P7 epilogue pipelining, KI tiling, gemv batching
# speedup vs baseline: 1.0220x; 1.0070x over previous
.LBB0_1194:
	s_waitcnt lgkmcnt(0)
	s_min_i32 s10, s97, 0xff
	v_and_b32_e32 v210, 15, v10
	v_ashrrev_i32_e32 v211, 4, v10
	v_lshl_add_u32 v2, v10, 1, s95
	v_cmp_lt_i32_e32 vcc, s10, v10
	s_and_saveexec_b64 s[0:1], vcc
	ds_write_b16 v2, v141
	s_or_b64 exec, exec, s[0:1]
	s_sub_i32 s13, s10, 63
	v_cmp_le_i32_e32 vcc, s13, v10
	s_and_saveexec_b64 s[0:1], vcc
	ds_write_b16 v2, v141 offset:128
	s_or_b64 exec, exec, s[0:1]
	s_add_i32 s12, s10, 0xffffff81
	v_cmp_le_i32_e32 vcc, s12, v10
	s_and_saveexec_b64 s[0:1], vcc
	ds_write_b16 v2, v141 offset:256
	s_or_b64 exec, exec, s[0:1]
	s_add_i32 s11, s10, 0xffffff41
	v_cmp_le_i32_e32 vcc, s11, v10
	s_and_saveexec_b64 s[0:1], vcc
	ds_write_b16 v2, v141 offset:384
	s_or_b64 exec, exec, s[0:1]
	s_add_i32 s0, s97, s25
	s_ashr_i32 s1, s0, 31
	s_waitcnt lgkmcnt(0)
	s_lshl_b64 s[8:9], s[0:1], 10
	v_readlane_b32 s14, v254, 60
	v_lshl_add_u32 v2, v210, 1, s95
	v_ashrrev_i32_e32 v213, 3, v10
	v_and_b32_e32 v214, 7, v10
	s_add_u32 s8, s14, s8
	v_readlane_b32 s14, v254, 61
	v_and_b32_e32 v120, 7, v210
	ds_read_u16 v15, v2
	ds_read_u16 v32, v2 offset:32
	ds_read_u16 v38, v2 offset:64
	ds_read_u16 v39, v2 offset:96
	ds_read_u16 v40, v2 offset:128
	ds_read_u16 v41, v2 offset:160
	ds_read_u16 v54, v2 offset:192
	ds_read_u16 v55, v2 offset:224
	ds_read_u16 v56, v2 offset:256
	ds_read_u16 v14, v2 offset:288
	ds_read_u16 v13, v2 offset:320
	ds_read_u16 v12, v2 offset:352
	ds_read_u16 v9, v2 offset:384
	ds_read_u16 v8, v2 offset:416
	ds_read_u16 v7, v2 offset:448
	ds_read_u16 v6, v2 offset:480
	s_addc_u32 s9, s14, s9
	v_lshl_add_u32 v212, v213, 1, s95
	v_lshlrev_b32_e32 v140, 7, v120
	v_lshlrev_b32_e32 v24, 4, v211
	ds_read_u16 v5, v212
	ds_read_u16 v4, v212 offset:16
	ds_read_u16 v11, v212 offset:32
	ds_read_u16 v10, v212 offset:48
	s_waitcnt lgkmcnt(0)
	v_lshl_add_u64 v[2:3], s[8:9], 0, v[140:141]
	v_ashrrev_i32_e32 v25, 31, v24
	v_lshl_add_u64 v[2:3], v[24:25], 1, v[2:3]
	global_load_dwordx4 v[16:19], v[2:3], off
	global_load_dwordx4 v[20:23], v[2:3], off offset:16
	v_lshl_add_u64 v[2:3], s[46:47], 0, v[24:25]
	s_waitcnt lgkmcnt(0)
	v_lshlrev_b32_e32 v140, 7, v15
	v_lshl_add_u64 v[244:245], v[2:3], 0, v[140:141]
	global_load_dwordx4 v[156:159], v[244:245], off
	global_load_dwordx4 v[160:163], v[244:245], off offset:64
	v_lshlrev_b32_e32 v140, 7, v32
	v_lshl_add_u64 v[244:245], v[2:3], 0, v[140:141]
	global_load_dwordx4 v[164:167], v[244:245], off
	global_load_dwordx4 v[168:171], v[244:245], off offset:64
	v_lshlrev_b32_e32 v140, 7, v38
	v_lshl_add_u64 v[244:245], v[2:3], 0, v[140:141]
	global_load_dwordx4 v[172:175], v[244:245], off
	global_load_dwordx4 v[176:179], v[244:245], off offset:64
	v_lshlrev_b32_e32 v140, 7, v39
	v_lshl_add_u64 v[244:245], v[2:3], 0, v[140:141]
	global_load_dwordx4 v[180:183], v[244:245], off
	global_load_dwordx4 v[184:187], v[244:245], off offset:64
	v_lshlrev_b32_e32 v140, 7, v40
	v_lshl_add_u64 v[244:245], v[2:3], 0, v[140:141]
	global_load_dwordx4 v[188:191], v[244:245], off
	global_load_dwordx4 v[192:195], v[244:245], off offset:64
	v_lshlrev_b32_e32 v140, 7, v41
	v_lshl_add_u64 v[244:245], v[2:3], 0, v[140:141]
	global_load_dwordx4 v[196:199], v[244:245], off
	global_load_dwordx4 v[224:227], v[244:245], off offset:64
	v_lshlrev_b32_e32 v140, 7, v54
	v_lshl_add_u64 v[244:245], v[2:3], 0, v[140:141]
	global_load_dwordx4 v[228:231], v[244:245], off
	global_load_dwordx4 v[232:235], v[244:245], off offset:64
	v_lshlrev_b32_e32 v140, 7, v55
	v_lshl_add_u64 v[244:245], v[2:3], 0, v[140:141]
	global_load_dwordx4 v[236:239], v[244:245], off
	global_load_dwordx4 v[240:243], v[244:245], off offset:64
	v_mov_b32_e32 v15, v141
	v_mov_b32_e32 v42, v141
	v_mov_b32_e32 v43, v141
	v_mov_b32_e32 v44, v141
	v_lshlrev_b32_e32 v116, 4, v214
	v_ashrrev_i32_e32 v117, 31, v116
	v_lshl_add_u64 v[114:115], s[48:49], 0, v[116:117]
	v_lshl_add_u32 v121, v211, 3, s95
	v_lshlrev_b32_e32 v117, 2, v211
	ds_read2_b64 v[110:113], v121 offset1:4
	ds_read2_b64 v[106:109], v121 offset0:8 offset1:12
	ds_read2_b64 v[102:105], v121 offset0:16 offset1:20
	ds_read2_b64 v[98:101], v121 offset0:24 offset1:28
	ds_read2_b64 v[94:97], v121 offset0:32 offset1:36
	ds_read2_b64 v[90:93], v121 offset0:40 offset1:44
	ds_read2_b64 v[86:89], v121 offset0:48 offset1:52
	s_waitcnt vmcnt(16)
	v_lshlrev_b32_e32 v45, 16, v16
	v_and_b32_e32 v16, 0xffff0000, v16
	v_lshlrev_b32_e32 v47, 16, v18
	v_and_b32_e32 v18, 0xffff0000, v18
	v_lshlrev_b32_e32 v49, 16, v20
	v_and_b32_e32 v20, 0xffff0000, v20
	v_lshlrev_b32_e32 v51, 16, v22
	v_and_b32_e32 v22, 0xffff0000, v22
	v_mul_f32_e32 v45, 0x41000000, v45
	v_mul_f32_e32 v16, 0x41000000, v16
	v_mul_f32_e32 v47, 0x41000000, v47
	v_mul_f32_e32 v18, 0x41000000, v18
	v_mul_f32_e32 v49, 0x41000000, v49
	v_mul_f32_e32 v20, 0x41000000, v20
	v_mul_f32_e32 v51, 0x41000000, v51
	v_mul_f32_e32 v22, 0x41000000, v22
	v_cvt_pk_fp8_f32 v15, v45, v16
	v_cvt_pk_fp8_f32 v42, v47, v18
	v_cvt_pk_fp8_f32 v43, v49, v20
	v_cvt_pk_fp8_f32 v44, v51, v22
	v_lshlrev_b32_e32 v46, 16, v17
	v_and_b32_e32 v17, 0xffff0000, v17
	v_lshlrev_b32_e32 v48, 16, v19
	v_and_b32_e32 v19, 0xffff0000, v19
	v_lshlrev_b32_e32 v50, 16, v21
	v_and_b32_e32 v21, 0xffff0000, v21
	v_lshlrev_b32_e32 v52, 16, v23
	v_and_b32_e32 v23, 0xffff0000, v23
	v_mul_f32_e32 v46, 0x41000000, v46
	v_mul_f32_e32 v17, 0x41000000, v17
	v_mul_f32_e32 v48, 0x41000000, v48
	v_mul_f32_e32 v19, 0x41000000, v19
	v_mul_f32_e32 v50, 0x41000000, v50
	v_mul_f32_e32 v21, 0x41000000, v21
	v_mul_f32_e32 v52, 0x41000000, v52
	v_mul_f32_e32 v23, 0x41000000, v23
	v_cvt_pk_fp8_f32 v15, v46, v17 op_sel:[0,0,1]
	v_cvt_pk_fp8_f32 v42, v48, v19 op_sel:[0,0,1]
	v_cvt_pk_fp8_f32 v43, v50, v21 op_sel:[0,0,1]
	v_cvt_pk_fp8_f32 v44, v52, v23 op_sel:[0,0,1]
	v_and_b32_e32 v20, -4, v210
	v_cmp_gt_u32_e32 vcc, 4, v210
	s_nop 1
	v_cndmask_b32_e32 v75, 0, v42, vcc
	v_cndmask_b32_e32 v74, 0, v15, vcc
	v_cndmask_b32_e32 v83, 0, v44, vcc
	v_cndmask_b32_e32 v82, 0, v43, vcc
	v_cmp_eq_u32_e32 vcc, 4, v20
	s_nop 1
	v_cndmask_b32_e32 v77, 0, v42, vcc
	v_cndmask_b32_e32 v76, 0, v15, vcc
	v_cndmask_b32_e32 v119, 0, v44, vcc
	v_cndmask_b32_e32 v118, 0, v43, vcc
	s_nop 1
	s_waitcnt vmcnt(14)
	v_mfma_f32_16x16x32_fp8_fp8 v[30:33], v[156:157], v[74:75], 0
	v_mfma_f32_16x16x32_fp8_fp8 v[30:33], v[158:159], v[82:83], v[30:33]
	v_mfma_f32_16x16x32_fp8_fp8 v[30:33], v[160:161], v[76:77], v[30:33]
	v_mfma_f32_16x16x32_fp8_fp8 v[30:33], v[162:163], v[118:119], v[30:33]
	v_lshlrev_b32_e32 v140, 7, v56
	v_lshl_add_u64 v[244:245], v[2:3], 0, v[140:141]
	global_load_dwordx4 v[156:159], v[244:245], off
	global_load_dwordx4 v[160:163], v[244:245], off offset:64
	s_waitcnt vmcnt(14)
	v_mfma_f32_16x16x32_fp8_fp8 v[42:45], v[164:165], v[74:75], 0
	v_mfma_f32_16x16x32_fp8_fp8 v[42:45], v[166:167], v[82:83], v[42:45]
	v_mfma_f32_16x16x32_fp8_fp8 v[42:45], v[168:169], v[76:77], v[42:45]
	v_mfma_f32_16x16x32_fp8_fp8 v[42:45], v[170:171], v[118:119], v[42:45]
	v_lshlrev_b32_e32 v140, 7, v14
	v_lshl_add_u64 v[244:245], v[2:3], 0, v[140:141]
	global_load_dwordx4 v[164:167], v[244:245], off
	global_load_dwordx4 v[168:171], v[244:245], off offset:64
	s_waitcnt vmcnt(14)
	v_mfma_f32_16x16x32_fp8_fp8 v[46:49], v[172:173], v[74:75], 0
	v_mfma_f32_16x16x32_fp8_fp8 v[46:49], v[174:175], v[82:83], v[46:49]
	v_mfma_f32_16x16x32_fp8_fp8 v[46:49], v[176:177], v[76:77], v[46:49]
	v_mfma_f32_16x16x32_fp8_fp8 v[46:49], v[178:179], v[118:119], v[46:49]
	v_lshlrev_b32_e32 v140, 7, v13
	v_lshl_add_u64 v[244:245], v[2:3], 0, v[140:141]
	global_load_dwordx4 v[172:175], v[244:245], off
	global_load_dwordx4 v[176:179], v[244:245], off offset:64
	s_waitcnt vmcnt(14)
	v_mfma_f32_16x16x32_fp8_fp8 v[50:53], v[180:181], v[74:75], 0
	v_mfma_f32_16x16x32_fp8_fp8 v[50:53], v[182:183], v[82:83], v[50:53]
	v_mfma_f32_16x16x32_fp8_fp8 v[50:53], v[184:185], v[76:77], v[50:53]
	v_mfma_f32_16x16x32_fp8_fp8 v[50:53], v[186:187], v[118:119], v[50:53]
	v_lshlrev_b32_e32 v140, 7, v12
	v_lshl_add_u64 v[244:245], v[2:3], 0, v[140:141]
	global_load_dwordx4 v[180:183], v[244:245], off
	global_load_dwordx4 v[184:187], v[244:245], off offset:64
	s_waitcnt vmcnt(14)
	v_mfma_f32_16x16x32_fp8_fp8 v[58:61], v[188:189], v[74:75], 0
	v_mfma_f32_16x16x32_fp8_fp8 v[58:61], v[190:191], v[82:83], v[58:61]
	v_mfma_f32_16x16x32_fp8_fp8 v[58:61], v[192:193], v[76:77], v[58:61]
	v_mfma_f32_16x16x32_fp8_fp8 v[58:61], v[194:195], v[118:119], v[58:61]
	v_lshlrev_b32_e32 v140, 7, v9
	v_lshl_add_u64 v[244:245], v[2:3], 0, v[140:141]
	global_load_dwordx4 v[188:191], v[244:245], off
	global_load_dwordx4 v[192:195], v[244:245], off offset:64
	s_waitcnt vmcnt(14)
	v_mfma_f32_16x16x32_fp8_fp8 v[62:65], v[196:197], v[74:75], 0
	v_mfma_f32_16x16x32_fp8_fp8 v[62:65], v[198:199], v[82:83], v[62:65]
	v_mfma_f32_16x16x32_fp8_fp8 v[62:65], v[224:225], v[76:77], v[62:65]
	v_mfma_f32_16x16x32_fp8_fp8 v[62:65], v[226:227], v[118:119], v[62:65]
	v_lshlrev_b32_e32 v140, 7, v8
	v_lshl_add_u64 v[244:245], v[2:3], 0, v[140:141]
	global_load_dwordx4 v[196:199], v[244:245], off
	global_load_dwordx4 v[224:227], v[244:245], off offset:64
	s_waitcnt vmcnt(14)
	v_mfma_f32_16x16x32_fp8_fp8 v[70:73], v[228:229], v[74:75], 0
	v_mfma_f32_16x16x32_fp8_fp8 v[70:73], v[230:231], v[82:83], v[70:73]
	v_mfma_f32_16x16x32_fp8_fp8 v[70:73], v[232:233], v[76:77], v[70:73]
	v_mfma_f32_16x16x32_fp8_fp8 v[70:73], v[234:235], v[118:119], v[70:73]
	v_lshlrev_b32_e32 v140, 7, v7
	v_lshl_add_u64 v[244:245], v[2:3], 0, v[140:141]
	global_load_dwordx4 v[228:231], v[244:245], off
	global_load_dwordx4 v[232:235], v[244:245], off offset:64
	s_waitcnt vmcnt(14)
	v_mfma_f32_16x16x32_fp8_fp8 v[78:81], v[236:237], v[74:75], 0
	v_mfma_f32_16x16x32_fp8_fp8 v[78:81], v[238:239], v[82:83], v[78:81]
	v_mfma_f32_16x16x32_fp8_fp8 v[78:81], v[240:241], v[76:77], v[78:81]
	v_mfma_f32_16x16x32_fp8_fp8 v[78:81], v[242:243], v[118:119], v[78:81]
	v_lshlrev_b32_e32 v140, 7, v6
	v_lshl_add_u64 v[244:245], v[2:3], 0, v[140:141]
	global_load_dwordx4 v[236:239], v[244:245], off
	global_load_dwordx4 v[240:243], v[244:245], off offset:64
	v_lshlrev_b32_e32 v140, 7, v5
	v_lshl_add_u64 v[246:247], v[114:115], 0, v[140:141]
	v_lshlrev_b32_e32 v140, 7, v4
	v_lshl_add_u64 v[248:249], v[114:115], 0, v[140:141]
	v_lshlrev_b32_e32 v140, 7, v11
	v_lshl_add_u64 v[250:251], v[114:115], 0, v[140:141]
	v_lshlrev_b32_e32 v140, 7, v10
	v_lshl_add_u64 v[252:253], v[114:115], 0, v[140:141]
	global_load_dwordx4 v[2:5], v[246:247], off
	global_load_dwordx4 v[6:9], v[248:249], off
	global_load_dwordx4 v[10:13], v[250:251], off
	global_load_dwordx4 v[14:17], v[252:253], off
	s_waitcnt vmcnt(18)
	v_mfma_f32_16x16x32_fp8_fp8 v[18:21], v[156:157], v[74:75], 0
	v_mfma_f32_16x16x32_fp8_fp8 v[18:21], v[158:159], v[82:83], v[18:21]
	v_mfma_f32_16x16x32_fp8_fp8 v[18:21], v[160:161], v[76:77], v[18:21]
	v_mfma_f32_16x16x32_fp8_fp8 v[18:21], v[162:163], v[118:119], v[18:21]
	s_waitcnt vmcnt(16)
	v_mfma_f32_16x16x32_fp8_fp8 v[22:25], v[164:165], v[74:75], 0
	v_mfma_f32_16x16x32_fp8_fp8 v[22:25], v[166:167], v[82:83], v[22:25]
	v_mfma_f32_16x16x32_fp8_fp8 v[22:25], v[168:169], v[76:77], v[22:25]
	v_mfma_f32_16x16x32_fp8_fp8 v[22:25], v[170:171], v[118:119], v[22:25]
	s_waitcnt vmcnt(14)
	v_mfma_f32_16x16x32_fp8_fp8 v[26:29], v[172:173], v[74:75], 0
	v_mfma_f32_16x16x32_fp8_fp8 v[26:29], v[174:175], v[82:83], v[26:29]
	v_mfma_f32_16x16x32_fp8_fp8 v[26:29], v[176:177], v[76:77], v[26:29]
	v_mfma_f32_16x16x32_fp8_fp8 v[26:29], v[178:179], v[118:119], v[26:29]
	s_waitcnt vmcnt(12)
	v_mfma_f32_16x16x32_fp8_fp8 v[34:37], v[180:181], v[74:75], 0
	v_mfma_f32_16x16x32_fp8_fp8 v[34:37], v[182:183], v[82:83], v[34:37]
	v_mfma_f32_16x16x32_fp8_fp8 v[34:37], v[184:185], v[76:77], v[34:37]
	v_mfma_f32_16x16x32_fp8_fp8 v[34:37], v[186:187], v[118:119], v[34:37]
	s_waitcnt vmcnt(10)
	v_mfma_f32_16x16x32_fp8_fp8 v[38:41], v[188:189], v[74:75], 0
	v_mfma_f32_16x16x32_fp8_fp8 v[38:41], v[190:191], v[82:83], v[38:41]
	v_mfma_f32_16x16x32_fp8_fp8 v[38:41], v[192:193], v[76:77], v[38:41]
	v_mfma_f32_16x16x32_fp8_fp8 v[38:41], v[194:195], v[118:119], v[38:41]
	s_waitcnt vmcnt(8)
	v_mfma_f32_16x16x32_fp8_fp8 v[54:57], v[196:197], v[74:75], 0
	v_mfma_f32_16x16x32_fp8_fp8 v[54:57], v[198:199], v[82:83], v[54:57]
	v_mfma_f32_16x16x32_fp8_fp8 v[54:57], v[224:225], v[76:77], v[54:57]
	v_mfma_f32_16x16x32_fp8_fp8 v[54:57], v[226:227], v[118:119], v[54:57]
	s_waitcnt vmcnt(6)
	v_mfma_f32_16x16x32_fp8_fp8 v[66:69], v[228:229], v[74:75], 0
	v_mfma_f32_16x16x32_fp8_fp8 v[66:69], v[230:231], v[82:83], v[66:69]
	v_mfma_f32_16x16x32_fp8_fp8 v[66:69], v[232:233], v[76:77], v[66:69]
	v_mfma_f32_16x16x32_fp8_fp8 v[66:69], v[234:235], v[118:119], v[66:69]
	s_waitcnt vmcnt(4)
	v_mfma_f32_16x16x32_fp8_fp8 v[248:251], v[236:237], v[74:75], 0
	v_mfma_f32_16x16x32_fp8_fp8 v[248:251], v[238:239], v[82:83], v[248:251]
	v_mfma_f32_16x16x32_fp8_fp8 v[74:77], v[240:241], v[76:77], v[248:251]
	v_mfma_f32_16x16x32_fp8_fp8 v[74:77], v[242:243], v[118:119], v[74:77]
	s_nop 7
	ds_read2_b64 v[82:85], v121 offset0:56 offset1:60
	v_lshl_add_u32 v140, v120, 2, s22
	s_waitcnt lgkmcnt(0)
	s_cmpk_lt_i32 s97, 0xff
	s_mov_b64 s[8:9], -1
	s_cbranch_scc0 .LBB0_1332
	v_cmp_ge_i32_e32 vcc, s10, v117
	v_mov_b32_e32 v119, 0xff800000
	v_mov_b32_e32 v118, 0xff800000
	s_and_saveexec_b64 s[8:9], vcc
	s_cbranch_execz .LBB0_1205
	s_waitcnt lgkmcnt(7)
	v_sub_u32_sdwa v118, s97, v110 dst_sel:DWORD dst_unused:UNUSED_PAD src0_sel:DWORD src1_sel:WORD_0
	v_min_i32_e32 v118, 0x71, v118
	v_lshl_add_u32 v118, v118, 5, v140
	ds_read_b32 v118, v118
	s_waitcnt lgkmcnt(0)
	v_fmac_f32_e32 v118, 0x3e000000, v30
